# P0 gate/up weight conversion: hand-written fast path with register double buffering (next item's 12 loads in flight during the LDS transpose of the current) + final RMSNorm rewrite
# baseline (speedup 1.0000x reference)
.LBB0_12:
	s_mov_b64 s[4:5], 0x1d00000
	v_lshl_add_u64 v[36:37], v[34:35], 0, s[4:5]
	s_ashr_i32 s6, s0, 6
	s_lshl_b32 s4, s1, 3
	s_add_i32 s4, s4, s6
	s_cmp_gt_i32 s4, 0x18daf
	v_and_b32_e32 v55, 63, v53
	s_cbranch_scc1 .LBB0_212
	s_load_dwordx2 s[30:31], s[90:91], 0xb8
	s_load_dwordx2 s[34:35], s[90:91], 0x30
	s_load_dwordx2 s[36:37], s[90:91], 0x78
	s_load_dwordx2 s[38:39], s[90:91], 0x40
	s_load_dwordx2 s[8:9], s[90:91], 0x58
	s_lshl_b32 s5, s3, 3
	s_mov_b64 s[40:41], 0x2000000
	s_cmp_lg_u64 s[18:19], 0
	v_lshl_add_u64 v[38:39], v[34:35], 0, s[40:41]
	s_cselect_b64 s[40:41], -1, 0
	s_mov_b64 s[42:43], 0x1c00000
	s_waitcnt lgkmcnt(0)
	s_cmp_lg_u64 s[38:39], 0
	v_lshl_add_u64 v[40:41], v[34:35], 0, s[42:43]
	s_cselect_b64 s[42:43], -1, 0
	s_add_u32 s33, s16, 0x1000
	s_addc_u32 s54, s17, 0
	s_mov_b64 s[44:45], 0x2b00000
	v_lshl_add_u64 v[42:43], v[34:35], 0, s[44:45]
	s_mov_b64 s[44:45], 0x2700000
	s_cmp_lg_u64 s[10:11], 0
	s_mov_b64 s[46:47], 0x2c00000
	v_lshl_add_u64 v[44:45], v[34:35], 0, s[44:45]
	s_cselect_b64 s[44:45], -1, 0
	v_lshl_add_u64 v[46:47], v[34:35], 0, s[46:47]
	s_mov_b64 s[46:47], 0xac00000
	s_lshl_b32 s6, s6, 14
	v_and_b32_e32 v1, 7, v53
	v_lshrrev_b32_e32 v57, 3, v55
	v_lshl_add_u64 v[48:49], v[34:35], 0, s[46:47]
	s_add_i32 s46, s6, 0
	v_lshlrev_b32_e32 v56, 3, v1
	v_mul_u32_u24_e32 v1, 0x420, v1
	v_lshlrev_b32_e32 v2, 2, v57
	v_add3_u32 v61, s46, v1, v2
	v_lshlrev_b32_e32 v1, 2, v55
	v_and_b32_e32 v60, 28, v1
	v_lshlrev_b32_e32 v58, 2, v60
	v_mul_u32_u24_e32 v1, 0x84, v57
	v_mov_b32_e32 v59, 0
	v_add3_u32 v87, s46, v58, v1
	v_and_b32_e32 v1, 3, v53
	v_or_b32_e32 v84, 8, v57
	v_or_b32_e32 v85, 16, v57
	v_or_b32_e32 v86, 24, v57
	v_lshlrev_b32_e32 v62, 4, v1
	v_lshrrev_b32_e32 v88, 2, v55
	v_mov_b32_e32 v63, v59
	v_and_b32_e32 v50, 31, v53
	v_lshrrev_b32_e32 v52, 5, v55
	v_lshlrev_b32_e32 v2, 10, v57
	v_lshlrev_b32_e32 v4, 10, v84
	v_lshlrev_b32_e32 v6, 10, v85
	v_lshlrev_b32_e32 v8, 10, v86
	v_mul_u32_u24_e32 v1, 0x840, v1
	v_lshl_add_u64 v[10:11], v[34:35], 0, v[62:63]
	s_mov_b64 s[48:49], 0x2300000
	v_and_b32_e32 v3, 60, v55
	v_or_b32_e32 v90, 16, v88
	v_lshl_add_u64 v[70:71], s[8:9], 0, v[58:59]
	s_mov_b64 s[8:9], 0x1e00000
	s_mov_b32 s47, 0
	v_lshl_add_u32 v54, v50, 2, s46
	v_cmp_gt_u32_e64 s[6:7], 16, v60
	s_movk_i32 s55, 0x84
	v_lshl_add_u64 v[64:65], v[10:11], 0, s[48:49]
	v_add3_u32 v89, s46, v1, v3
	v_lshlrev_b32_e32 v66, 10, v88
	v_mov_b32_e32 v67, v59
	v_lshlrev_b32_e32 v68, 10, v90
	v_mov_b32_e32 v69, v59
	v_lshl_add_u64 v[72:73], v[10:11], 0, s[8:9]
	v_mov_b32_e32 v1, v52
	s_movk_i32 s56, 0x7fff
	s_mov_b32 s57, 0xffff0000
	v_lshlrev_b32_e32 v74, 1, v2
	v_lshlrev_b32_e32 v76, 1, v4
	v_lshlrev_b32_e32 v78, 1, v6
	v_lshlrev_b32_e32 v80, 1, v8
	s_mov_b32 s64, 0x8000
	s_mov_b32 s65, 0x10000
	s_mov_b32 s66, 0x18000
	s_mov_b32 s67, 0x20000
	s_mov_b32 s68, 0x28000
	s_mov_b32 s69, 0x30000
	s_mov_b32 s70, 0x38000
	s_mov_b32 s71, 0x40000
	s_mov_b32 s72, 0x50000
	s_mov_b32 s73, 0x60000
	s_mov_b32 s74, 0x70000
	v_mov_b32_e32 v91, 0x41800000
	v_mov_b32_e32 v92, 0x421d265f
	v_mov_b32_e32 v51, v50
	s_add_i32 s32, s4, s5
	s_cmp_lt_u32 s32, 0x10000
	s_cbranch_scc0 .Lcv_skip
	v_lshlrev_b32_e32 v240, 13, v57
	v_lshl_add_u32 v240, v60, 2, v240
	v_add_u32_e32 v241, 0x10000, v240
	v_add_u32_e32 v242, 0x20000, v240
	v_add_u32_e32 v243, 0x30000, v240
	v_add_u32_e32 v244, 0x40000, v240
	v_add_u32_e32 v245, 0x50000, v240
	v_add_u32_e32 v246, 0x60000, v240
	v_add_u32_e32 v247, 0x70000, v240
	v_mov_b32_e32 v248, v87
	v_add_u32_e32 v249, 0x420, v87
	v_add_u32_e32 v250, 0x840, v87
	v_add_u32_e32 v251, 0xc60, v87
	v_add_u32_e32 v252, 0x1080, v87
	v_add_u32_e32 v253, 0x14a0, v87
	v_add_u32_e32 v118, 0x18c0, v87
	v_add_u32_e32 v119, 0x1ce0, v87
	v_lshl_add_u32 v120, v88, 10, v62
	v_add_u32_e32 v121, 0x4000, v120
	v_lshlrev_b32_e32 v122, 2, v62
	v_add_u32_e32 v124, 0x400, v89
	s_lshr_b32 s86, s4, 10
	s_and_b32 s87, s4, 0x3c0
	s_lshl_b32 s88, s86, 23
	s_lshl_b32 s89, s87, 13
	s_add_u32 s88, s88, s89
	s_lshl_b32 s89, s4, 7
	s_and_b32 s89, s89, 0x1f80
	s_add_u32 s88, s88, s89
	s_add_u32 s92, s20, s88
	s_addc_u32 s93, s21, 0
	global_load_dwordx4 v[160:163], v240, s[92:93]
	global_load_dwordx4 v[164:167], v241, s[92:93]
	global_load_dwordx4 v[168:171], v242, s[92:93]
	global_load_dwordx4 v[172:175], v243, s[92:93]
	global_load_dwordx4 v[176:179], v244, s[92:93]
	global_load_dwordx4 v[180:183], v245, s[92:93]
	global_load_dwordx4 v[184:187], v246, s[92:93]
	global_load_dwordx4 v[188:191], v247, s[92:93]
	s_lshr_b32 s88, s86, 5
	s_lshl_b32 s88, s88, 12
	s_lshl_b32 s89, s87, 2
	s_add_u32 s88, s88, s89
	s_add_u32 s96, s18, s88
	s_addc_u32 s97, s19, 0
	global_load_dwordx4 v[224:227], v122, s[96:97] offset:0
	global_load_dwordx4 v[228:231], v122, s[96:97] offset:16
	global_load_dwordx4 v[232:235], v122, s[96:97] offset:32
	global_load_dwordx4 v[236:239], v122, s[96:97] offset:48
.Lcv_loop:
	s_add_i32 s32, s4, s5
	s_cmp_lt_u32 s32, 0x10000
	s_cbranch_scc0 .Lcv_tail0
	s_lshr_b32 s86, s32, 10
	s_and_b32 s87, s32, 0x3c0
	s_lshl_b32 s88, s86, 23
	s_lshl_b32 s89, s87, 13
	s_add_u32 s88, s88, s89
	s_lshl_b32 s89, s32, 7
	s_and_b32 s89, s89, 0x1f80
	s_add_u32 s88, s88, s89
	s_add_u32 s92, s20, s88
	s_addc_u32 s93, s21, 0
	global_load_dwordx4 v[192:195], v240, s[92:93]
	global_load_dwordx4 v[196:199], v241, s[92:93]
	global_load_dwordx4 v[200:203], v242, s[92:93]
	global_load_dwordx4 v[204:207], v243, s[92:93]
	global_load_dwordx4 v[208:211], v244, s[92:93]
	global_load_dwordx4 v[212:215], v245, s[92:93]
	global_load_dwordx4 v[216:219], v246, s[92:93]
	global_load_dwordx4 v[220:223], v247, s[92:93]
	s_lshr_b32 s88, s86, 5
	s_lshl_b32 s88, s88, 12
	s_lshl_b32 s89, s87, 2
	s_add_u32 s88, s88, s89
	s_add_u32 s96, s18, s88
	s_addc_u32 s97, s19, 0
	global_load_dwordx4 v[136:139], v122, s[96:97] offset:0
	global_load_dwordx4 v[140:143], v122, s[96:97] offset:16
	global_load_dwordx4 v[144:147], v122, s[96:97] offset:32
	global_load_dwordx4 v[148:151], v122, s[96:97] offset:48
	s_waitcnt vmcnt(12)
	s_lshr_b32 s86, s4, 10
	s_and_b32 s87, s4, 0x3c0
	s_lshl_b32 s88, s86, 21
	s_add_u32 s88, s88, s87
	s_lshl_b32 s89, s4, 6
	s_and_b32 s89, s89, 0x7c0
	s_and_b32 s95, s4, 32
	s_or_b32 s89, s89, s95
	s_lshl_b32 s89, s89, 10
	s_add_u32 s88, s88, s89
	s_add_u32 s88, s88, 0xac00000
	s_add_u32 s96, s52, s88
	s_addc_u32 s97, s53, 0
	s_and_b32 s95, s4, 32
	s_cmp_eq_u32 s95, 0
	s_mov_b32 s95, 0x41800000
	s_cmov_b32 s95, 0x421d265f
	ds_write2_b32 v248, v160, v161 offset1:1
	ds_write2_b32 v248, v162, v163 offset0:2 offset1:3
	ds_write2_b32 v249, v164, v165 offset1:1
	ds_write2_b32 v249, v166, v167 offset0:2 offset1:3
	ds_write2_b32 v250, v168, v169 offset1:1
	ds_write2_b32 v250, v170, v171 offset0:2 offset1:3
	ds_write2_b32 v251, v172, v173 offset1:1
	ds_write2_b32 v251, v174, v175 offset0:2 offset1:3
	ds_write2_b32 v252, v176, v177 offset1:1
	ds_write2_b32 v252, v178, v179 offset0:2 offset1:3
	ds_write2_b32 v253, v180, v181 offset1:1
	ds_write2_b32 v253, v182, v183 offset0:2 offset1:3
	ds_write2_b32 v118, v184, v185 offset1:1
	ds_write2_b32 v118, v186, v187 offset0:2 offset1:3
	ds_write2_b32 v119, v188, v189 offset1:1
	ds_write2_b32 v119, v190, v191 offset0:2 offset1:3
	v_mul_f32_e32 v224, s95, v224
	v_mul_f32_e32 v225, s95, v225
	v_mul_f32_e32 v226, s95, v226
	v_mul_f32_e32 v227, s95, v227
	v_mul_f32_e32 v228, s95, v228
	v_mul_f32_e32 v229, s95, v229
	v_mul_f32_e32 v230, s95, v230
	v_mul_f32_e32 v231, s95, v231
	v_mul_f32_e32 v232, s95, v232
	v_mul_f32_e32 v233, s95, v233
	v_mul_f32_e32 v234, s95, v234
	v_mul_f32_e32 v235, s95, v235
	v_mul_f32_e32 v236, s95, v236
	v_mul_f32_e32 v237, s95, v237
	v_mul_f32_e32 v238, s95, v238
	v_mul_f32_e32 v239, s95, v239
	s_waitcnt lgkmcnt(0)
	ds_read2_b32 v[160:161], v89 offset0:0 offset1:16
	ds_read2_b32 v[162:163], v89 offset0:33 offset1:49
	ds_read2_b32 v[164:165], v89 offset0:66 offset1:82
	ds_read2_b32 v[166:167], v89 offset0:99 offset1:115
	ds_read2_b32 v[168:169], v89 offset0:132 offset1:148
	ds_read2_b32 v[170:171], v89 offset0:165 offset1:181
	ds_read2_b32 v[172:173], v89 offset0:198 offset1:214
	ds_read2_b32 v[174:175], v89 offset0:231 offset1:247
	ds_read2_b32 v[176:177], v124 offset0:8 offset1:24
	ds_read2_b32 v[178:179], v124 offset0:41 offset1:57
	ds_read2_b32 v[180:181], v124 offset0:74 offset1:90
	ds_read2_b32 v[182:183], v124 offset0:107 offset1:123
	ds_read2_b32 v[184:185], v124 offset0:140 offset1:156
	ds_read2_b32 v[186:187], v124 offset0:173 offset1:189
	ds_read2_b32 v[188:189], v124 offset0:206 offset1:222
	ds_read2_b32 v[190:191], v124 offset0:239 offset1:255
	s_waitcnt lgkmcnt(12)
	v_mul_f32_e32 v160, v224, v160
	v_mul_f32_e32 v161, v224, v161
	v_mul_f32_e32 v162, v225, v162
	v_mul_f32_e32 v163, v225, v163
	v_mul_f32_e32 v164, v226, v164
	v_mul_f32_e32 v165, v226, v165
	v_mul_f32_e32 v166, v227, v166
	v_mul_f32_e32 v167, v227, v167
	v_cvt_pk_fp8_f32 v128, v160, v162
	v_cvt_pk_fp8_f32 v132, v161, v163
	s_nop 0
	v_cvt_pk_fp8_f32 v128, v164, v166 op_sel:[0,0,1]
	v_cvt_pk_fp8_f32 v132, v165, v167 op_sel:[0,0,1]
	s_waitcnt lgkmcnt(8)
	v_mul_f32_e32 v168, v228, v168
	v_mul_f32_e32 v169, v228, v169
	v_mul_f32_e32 v170, v229, v170
	v_mul_f32_e32 v171, v229, v171
	v_mul_f32_e32 v172, v230, v172
	v_mul_f32_e32 v173, v230, v173
	v_mul_f32_e32 v174, v231, v174
	v_mul_f32_e32 v175, v231, v175
	v_cvt_pk_fp8_f32 v129, v168, v170
	v_cvt_pk_fp8_f32 v133, v169, v171
	s_nop 0
	v_cvt_pk_fp8_f32 v129, v172, v174 op_sel:[0,0,1]
	v_cvt_pk_fp8_f32 v133, v173, v175 op_sel:[0,0,1]
	s_waitcnt lgkmcnt(4)
	v_mul_f32_e32 v176, v232, v176
	v_mul_f32_e32 v177, v232, v177
	v_mul_f32_e32 v178, v233, v178
	v_mul_f32_e32 v179, v233, v179
	v_mul_f32_e32 v180, v234, v180
	v_mul_f32_e32 v181, v234, v181
	v_mul_f32_e32 v182, v235, v182
	v_mul_f32_e32 v183, v235, v183
	v_cvt_pk_fp8_f32 v130, v176, v178
	v_cvt_pk_fp8_f32 v134, v177, v179
	s_nop 0
	v_cvt_pk_fp8_f32 v130, v180, v182 op_sel:[0,0,1]
	v_cvt_pk_fp8_f32 v134, v181, v183 op_sel:[0,0,1]
	s_waitcnt lgkmcnt(0)
	v_mul_f32_e32 v184, v236, v184
	v_mul_f32_e32 v185, v236, v185
	v_mul_f32_e32 v186, v237, v186
	v_mul_f32_e32 v187, v237, v187
	v_mul_f32_e32 v188, v238, v188
	v_mul_f32_e32 v189, v238, v189
	v_mul_f32_e32 v190, v239, v190
	v_mul_f32_e32 v191, v239, v191
	v_cvt_pk_fp8_f32 v131, v184, v186
	v_cvt_pk_fp8_f32 v135, v185, v187
	s_nop 0
	v_cvt_pk_fp8_f32 v131, v188, v190 op_sel:[0,0,1]
	v_cvt_pk_fp8_f32 v135, v189, v191 op_sel:[0,0,1]
	s_nop 0
	global_store_dwordx4 v120, v[128:131], s[96:97]
	global_store_dwordx4 v121, v[132:135], s[96:97]
	s_add_i32 s4, s4, s5
	s_add_i32 s32, s4, s5
	s_cmp_lt_u32 s32, 0x10000
	s_cbranch_scc0 .Lcv_tail1
	s_lshr_b32 s86, s32, 10
	s_and_b32 s87, s32, 0x3c0
	s_lshl_b32 s88, s86, 23
	s_lshl_b32 s89, s87, 13
	s_add_u32 s88, s88, s89
	s_lshl_b32 s89, s32, 7
	s_and_b32 s89, s89, 0x1f80
	s_add_u32 s88, s88, s89
	s_add_u32 s92, s20, s88
	s_addc_u32 s93, s21, 0
	global_load_dwordx4 v[160:163], v240, s[92:93]
	global_load_dwordx4 v[164:167], v241, s[92:93]
	global_load_dwordx4 v[168:171], v242, s[92:93]
	global_load_dwordx4 v[172:175], v243, s[92:93]
	global_load_dwordx4 v[176:179], v244, s[92:93]
	global_load_dwordx4 v[180:183], v245, s[92:93]
	global_load_dwordx4 v[184:187], v246, s[92:93]
	global_load_dwordx4 v[188:191], v247, s[92:93]
	s_lshr_b32 s88, s86, 5
	s_lshl_b32 s88, s88, 12
	s_lshl_b32 s89, s87, 2
	s_add_u32 s88, s88, s89
	s_add_u32 s96, s18, s88
	s_addc_u32 s97, s19, 0
	global_load_dwordx4 v[224:227], v122, s[96:97] offset:0
	global_load_dwordx4 v[228:231], v122, s[96:97] offset:16
	global_load_dwordx4 v[232:235], v122, s[96:97] offset:32
	global_load_dwordx4 v[236:239], v122, s[96:97] offset:48
	s_waitcnt vmcnt(12)
	s_lshr_b32 s86, s4, 10
	s_and_b32 s87, s4, 0x3c0
	s_lshl_b32 s88, s86, 21
	s_add_u32 s88, s88, s87
	s_lshl_b32 s89, s4, 6
	s_and_b32 s89, s89, 0x7c0
	s_and_b32 s95, s4, 32
	s_or_b32 s89, s89, s95
	s_lshl_b32 s89, s89, 10
	s_add_u32 s88, s88, s89
	s_add_u32 s88, s88, 0xac00000
	s_add_u32 s96, s52, s88
	s_addc_u32 s97, s53, 0
	s_and_b32 s95, s4, 32
	s_cmp_eq_u32 s95, 0
	s_mov_b32 s95, 0x41800000
	s_cmov_b32 s95, 0x421d265f
	ds_write2_b32 v248, v192, v193 offset1:1
	ds_write2_b32 v248, v194, v195 offset0:2 offset1:3
	ds_write2_b32 v249, v196, v197 offset1:1
	ds_write2_b32 v249, v198, v199 offset0:2 offset1:3
	ds_write2_b32 v250, v200, v201 offset1:1
	ds_write2_b32 v250, v202, v203 offset0:2 offset1:3
	ds_write2_b32 v251, v204, v205 offset1:1
	ds_write2_b32 v251, v206, v207 offset0:2 offset1:3
	ds_write2_b32 v252, v208, v209 offset1:1
	ds_write2_b32 v252, v210, v211 offset0:2 offset1:3
	ds_write2_b32 v253, v212, v213 offset1:1
	ds_write2_b32 v253, v214, v215 offset0:2 offset1:3
	ds_write2_b32 v118, v216, v217 offset1:1
	ds_write2_b32 v118, v218, v219 offset0:2 offset1:3
	ds_write2_b32 v119, v220, v221 offset1:1
	ds_write2_b32 v119, v222, v223 offset0:2 offset1:3
	v_mul_f32_e32 v136, s95, v136
	v_mul_f32_e32 v137, s95, v137
	v_mul_f32_e32 v138, s95, v138
	v_mul_f32_e32 v139, s95, v139
	v_mul_f32_e32 v140, s95, v140
	v_mul_f32_e32 v141, s95, v141
	v_mul_f32_e32 v142, s95, v142
	v_mul_f32_e32 v143, s95, v143
	v_mul_f32_e32 v144, s95, v144
	v_mul_f32_e32 v145, s95, v145
	v_mul_f32_e32 v146, s95, v146
	v_mul_f32_e32 v147, s95, v147
	v_mul_f32_e32 v148, s95, v148
	v_mul_f32_e32 v149, s95, v149
	v_mul_f32_e32 v150, s95, v150
	v_mul_f32_e32 v151, s95, v151
	s_waitcnt lgkmcnt(0)
	ds_read2_b32 v[192:193], v89 offset0:0 offset1:16
	ds_read2_b32 v[194:195], v89 offset0:33 offset1:49
	ds_read2_b32 v[196:197], v89 offset0:66 offset1:82
	ds_read2_b32 v[198:199], v89 offset0:99 offset1:115
	ds_read2_b32 v[200:201], v89 offset0:132 offset1:148
	ds_read2_b32 v[202:203], v89 offset0:165 offset1:181
	ds_read2_b32 v[204:205], v89 offset0:198 offset1:214
	ds_read2_b32 v[206:207], v89 offset0:231 offset1:247
	ds_read2_b32 v[208:209], v124 offset0:8 offset1:24
	ds_read2_b32 v[210:211], v124 offset0:41 offset1:57
	ds_read2_b32 v[212:213], v124 offset0:74 offset1:90
	ds_read2_b32 v[214:215], v124 offset0:107 offset1:123
	ds_read2_b32 v[216:217], v124 offset0:140 offset1:156
	ds_read2_b32 v[218:219], v124 offset0:173 offset1:189
	ds_read2_b32 v[220:221], v124 offset0:206 offset1:222
	ds_read2_b32 v[222:223], v124 offset0:239 offset1:255
	s_waitcnt lgkmcnt(12)
	v_mul_f32_e32 v192, v136, v192
	v_mul_f32_e32 v193, v136, v193
	v_mul_f32_e32 v194, v137, v194
	v_mul_f32_e32 v195, v137, v195
	v_mul_f32_e32 v196, v138, v196
	v_mul_f32_e32 v197, v138, v197
	v_mul_f32_e32 v198, v139, v198
	v_mul_f32_e32 v199, v139, v199
	v_cvt_pk_fp8_f32 v128, v192, v194
	v_cvt_pk_fp8_f32 v132, v193, v195
	s_nop 0
	v_cvt_pk_fp8_f32 v128, v196, v198 op_sel:[0,0,1]
	v_cvt_pk_fp8_f32 v132, v197, v199 op_sel:[0,0,1]
	s_waitcnt lgkmcnt(8)
	v_mul_f32_e32 v200, v140, v200
	v_mul_f32_e32 v201, v140, v201
	v_mul_f32_e32 v202, v141, v202
	v_mul_f32_e32 v203, v141, v203
	v_mul_f32_e32 v204, v142, v204
	v_mul_f32_e32 v205, v142, v205
	v_mul_f32_e32 v206, v143, v206
	v_mul_f32_e32 v207, v143, v207
	v_cvt_pk_fp8_f32 v129, v200, v202
	v_cvt_pk_fp8_f32 v133, v201, v203
	s_nop 0
	v_cvt_pk_fp8_f32 v129, v204, v206 op_sel:[0,0,1]
	v_cvt_pk_fp8_f32 v133, v205, v207 op_sel:[0,0,1]
	s_waitcnt lgkmcnt(4)
	v_mul_f32_e32 v208, v144, v208
	v_mul_f32_e32 v209, v144, v209
	v_mul_f32_e32 v210, v145, v210
	v_mul_f32_e32 v211, v145, v211
	v_mul_f32_e32 v212, v146, v212
	v_mul_f32_e32 v213, v146, v213
	v_mul_f32_e32 v214, v147, v214
	v_mul_f32_e32 v215, v147, v215
	v_cvt_pk_fp8_f32 v130, v208, v210
	v_cvt_pk_fp8_f32 v134, v209, v211
	s_nop 0
	v_cvt_pk_fp8_f32 v130, v212, v214 op_sel:[0,0,1]
	v_cvt_pk_fp8_f32 v134, v213, v215 op_sel:[0,0,1]
	s_waitcnt lgkmcnt(0)
	v_mul_f32_e32 v216, v148, v216
	v_mul_f32_e32 v217, v148, v217
	v_mul_f32_e32 v218, v149, v218
	v_mul_f32_e32 v219, v149, v219
	v_mul_f32_e32 v220, v150, v220
	v_mul_f32_e32 v221, v150, v221
	v_mul_f32_e32 v222, v151, v222
	v_mul_f32_e32 v223, v151, v223
	v_cvt_pk_fp8_f32 v131, v216, v218
	v_cvt_pk_fp8_f32 v135, v217, v219
	s_nop 0
	v_cvt_pk_fp8_f32 v131, v220, v222 op_sel:[0,0,1]
	v_cvt_pk_fp8_f32 v135, v221, v223 op_sel:[0,0,1]
	s_nop 0
	global_store_dwordx4 v120, v[128:131], s[96:97]
	global_store_dwordx4 v121, v[132:135], s[96:97]
	s_add_i32 s4, s4, s5
	s_branch .Lcv_loop
.Lcv_tail0:
	s_waitcnt vmcnt(0)
	s_lshr_b32 s86, s4, 10
	s_and_b32 s87, s4, 0x3c0
	s_lshl_b32 s88, s86, 21
	s_add_u32 s88, s88, s87
	s_lshl_b32 s89, s4, 6
	s_and_b32 s89, s89, 0x7c0
	s_and_b32 s95, s4, 32
	s_or_b32 s89, s89, s95
	s_lshl_b32 s89, s89, 10
	s_add_u32 s88, s88, s89
	s_add_u32 s88, s88, 0xac00000
	s_add_u32 s96, s52, s88
	s_addc_u32 s97, s53, 0
	s_and_b32 s95, s4, 32
	s_cmp_eq_u32 s95, 0
	s_mov_b32 s95, 0x41800000
	s_cmov_b32 s95, 0x421d265f
	ds_write2_b32 v248, v160, v161 offset1:1
	ds_write2_b32 v248, v162, v163 offset0:2 offset1:3
	ds_write2_b32 v249, v164, v165 offset1:1
	ds_write2_b32 v249, v166, v167 offset0:2 offset1:3
	ds_write2_b32 v250, v168, v169 offset1:1
	ds_write2_b32 v250, v170, v171 offset0:2 offset1:3
	ds_write2_b32 v251, v172, v173 offset1:1
	ds_write2_b32 v251, v174, v175 offset0:2 offset1:3
	ds_write2_b32 v252, v176, v177 offset1:1
	ds_write2_b32 v252, v178, v179 offset0:2 offset1:3
	ds_write2_b32 v253, v180, v181 offset1:1
	ds_write2_b32 v253, v182, v183 offset0:2 offset1:3
	ds_write2_b32 v118, v184, v185 offset1:1
	ds_write2_b32 v118, v186, v187 offset0:2 offset1:3
	ds_write2_b32 v119, v188, v189 offset1:1
	ds_write2_b32 v119, v190, v191 offset0:2 offset1:3
	v_mul_f32_e32 v224, s95, v224
	v_mul_f32_e32 v225, s95, v225
	v_mul_f32_e32 v226, s95, v226
	v_mul_f32_e32 v227, s95, v227
	v_mul_f32_e32 v228, s95, v228
	v_mul_f32_e32 v229, s95, v229
	v_mul_f32_e32 v230, s95, v230
	v_mul_f32_e32 v231, s95, v231
	v_mul_f32_e32 v232, s95, v232
	v_mul_f32_e32 v233, s95, v233
	v_mul_f32_e32 v234, s95, v234
	v_mul_f32_e32 v235, s95, v235
	v_mul_f32_e32 v236, s95, v236
	v_mul_f32_e32 v237, s95, v237
	v_mul_f32_e32 v238, s95, v238
	v_mul_f32_e32 v239, s95, v239
	s_waitcnt lgkmcnt(0)
	ds_read2_b32 v[160:161], v89 offset0:0 offset1:16
	ds_read2_b32 v[162:163], v89 offset0:33 offset1:49
	ds_read2_b32 v[164:165], v89 offset0:66 offset1:82
	ds_read2_b32 v[166:167], v89 offset0:99 offset1:115
	ds_read2_b32 v[168:169], v89 offset0:132 offset1:148
	ds_read2_b32 v[170:171], v89 offset0:165 offset1:181
	ds_read2_b32 v[172:173], v89 offset0:198 offset1:214
	ds_read2_b32 v[174:175], v89 offset0:231 offset1:247
	ds_read2_b32 v[176:177], v124 offset0:8 offset1:24
	ds_read2_b32 v[178:179], v124 offset0:41 offset1:57
	ds_read2_b32 v[180:181], v124 offset0:74 offset1:90
	ds_read2_b32 v[182:183], v124 offset0:107 offset1:123
	ds_read2_b32 v[184:185], v124 offset0:140 offset1:156
	ds_read2_b32 v[186:187], v124 offset0:173 offset1:189
	ds_read2_b32 v[188:189], v124 offset0:206 offset1:222
	ds_read2_b32 v[190:191], v124 offset0:239 offset1:255
	s_waitcnt lgkmcnt(12)
	v_mul_f32_e32 v160, v224, v160
	v_mul_f32_e32 v161, v224, v161
	v_mul_f32_e32 v162, v225, v162
	v_mul_f32_e32 v163, v225, v163
	v_mul_f32_e32 v164, v226, v164
	v_mul_f32_e32 v165, v226, v165
	v_mul_f32_e32 v166, v227, v166
	v_mul_f32_e32 v167, v227, v167
	v_cvt_pk_fp8_f32 v128, v160, v162
	v_cvt_pk_fp8_f32 v132, v161, v163
	s_nop 0
	v_cvt_pk_fp8_f32 v128, v164, v166 op_sel:[0,0,1]
	v_cvt_pk_fp8_f32 v132, v165, v167 op_sel:[0,0,1]
	s_waitcnt lgkmcnt(8)
	v_mul_f32_e32 v168, v228, v168
	v_mul_f32_e32 v169, v228, v169
	v_mul_f32_e32 v170, v229, v170
	v_mul_f32_e32 v171, v229, v171
	v_mul_f32_e32 v172, v230, v172
	v_mul_f32_e32 v173, v230, v173
	v_mul_f32_e32 v174, v231, v174
	v_mul_f32_e32 v175, v231, v175
	v_cvt_pk_fp8_f32 v129, v168, v170
	v_cvt_pk_fp8_f32 v133, v169, v171
	s_nop 0
	v_cvt_pk_fp8_f32 v129, v172, v174 op_sel:[0,0,1]
	v_cvt_pk_fp8_f32 v133, v173, v175 op_sel:[0,0,1]
	s_waitcnt lgkmcnt(4)
	v_mul_f32_e32 v176, v232, v176
	v_mul_f32_e32 v177, v232, v177
	v_mul_f32_e32 v178, v233, v178
	v_mul_f32_e32 v179, v233, v179
	v_mul_f32_e32 v180, v234, v180
	v_mul_f32_e32 v181, v234, v181
	v_mul_f32_e32 v182, v235, v182
	v_mul_f32_e32 v183, v235, v183
	v_cvt_pk_fp8_f32 v130, v176, v178
	v_cvt_pk_fp8_f32 v134, v177, v179
	s_nop 0
	v_cvt_pk_fp8_f32 v130, v180, v182 op_sel:[0,0,1]
	v_cvt_pk_fp8_f32 v134, v181, v183 op_sel:[0,0,1]
	s_waitcnt lgkmcnt(0)
	v_mul_f32_e32 v184, v236, v184
	v_mul_f32_e32 v185, v236, v185
	v_mul_f32_e32 v186, v237, v186
	v_mul_f32_e32 v187, v237, v187
	v_mul_f32_e32 v188, v238, v188
	v_mul_f32_e32 v189, v238, v189
	v_mul_f32_e32 v190, v239, v190
	v_mul_f32_e32 v191, v239, v191
	v_cvt_pk_fp8_f32 v131, v184, v186
	v_cvt_pk_fp8_f32 v135, v185, v187
	s_nop 0
	v_cvt_pk_fp8_f32 v131, v188, v190 op_sel:[0,0,1]
	v_cvt_pk_fp8_f32 v135, v189, v191 op_sel:[0,0,1]
	s_nop 0
	global_store_dwordx4 v120, v[128:131], s[96:97]
	global_store_dwordx4 v121, v[132:135], s[96:97]
	s_add_i32 s4, s4, s5
	s_branch .Lcv_done
.Lcv_tail1:
	s_waitcnt vmcnt(0)
	s_lshr_b32 s86, s4, 10
	s_and_b32 s87, s4, 0x3c0
	s_lshl_b32 s88, s86, 21
	s_add_u32 s88, s88, s87
	s_lshl_b32 s89, s4, 6
	s_and_b32 s89, s89, 0x7c0
	s_and_b32 s95, s4, 32
	s_or_b32 s89, s89, s95
	s_lshl_b32 s89, s89, 10
	s_add_u32 s88, s88, s89
	s_add_u32 s88, s88, 0xac00000
	s_add_u32 s96, s52, s88
	s_addc_u32 s97, s53, 0
	s_and_b32 s95, s4, 32
	s_cmp_eq_u32 s95, 0
	s_mov_b32 s95, 0x41800000
	s_cmov_b32 s95, 0x421d265f
	ds_write2_b32 v248, v192, v193 offset1:1
	ds_write2_b32 v248, v194, v195 offset0:2 offset1:3
	ds_write2_b32 v249, v196, v197 offset1:1
	ds_write2_b32 v249, v198, v199 offset0:2 offset1:3
	ds_write2_b32 v250, v200, v201 offset1:1
	ds_write2_b32 v250, v202, v203 offset0:2 offset1:3
	ds_write2_b32 v251, v204, v205 offset1:1
	ds_write2_b32 v251, v206, v207 offset0:2 offset1:3
	ds_write2_b32 v252, v208, v209 offset1:1
	ds_write2_b32 v252, v210, v211 offset0:2 offset1:3
	ds_write2_b32 v253, v212, v213 offset1:1
	ds_write2_b32 v253, v214, v215 offset0:2 offset1:3
	ds_write2_b32 v118, v216, v217 offset1:1
	ds_write2_b32 v118, v218, v219 offset0:2 offset1:3
	ds_write2_b32 v119, v220, v221 offset1:1
	ds_write2_b32 v119, v222, v223 offset0:2 offset1:3
	v_mul_f32_e32 v136, s95, v136
	v_mul_f32_e32 v137, s95, v137
	v_mul_f32_e32 v138, s95, v138
	v_mul_f32_e32 v139, s95, v139
	v_mul_f32_e32 v140, s95, v140
	v_mul_f32_e32 v141, s95, v141
	v_mul_f32_e32 v142, s95, v142
	v_mul_f32_e32 v143, s95, v143
	v_mul_f32_e32 v144, s95, v144
	v_mul_f32_e32 v145, s95, v145
	v_mul_f32_e32 v146, s95, v146
	v_mul_f32_e32 v147, s95, v147
	v_mul_f32_e32 v148, s95, v148
	v_mul_f32_e32 v149, s95, v149
	v_mul_f32_e32 v150, s95, v150
	v_mul_f32_e32 v151, s95, v151
	s_waitcnt lgkmcnt(0)
	ds_read2_b32 v[192:193], v89 offset0:0 offset1:16
	ds_read2_b32 v[194:195], v89 offset0:33 offset1:49
	ds_read2_b32 v[196:197], v89 offset0:66 offset1:82
	ds_read2_b32 v[198:199], v89 offset0:99 offset1:115
	ds_read2_b32 v[200:201], v89 offset0:132 offset1:148
	ds_read2_b32 v[202:203], v89 offset0:165 offset1:181
	ds_read2_b32 v[204:205], v89 offset0:198 offset1:214
	ds_read2_b32 v[206:207], v89 offset0:231 offset1:247
	ds_read2_b32 v[208:209], v124 offset0:8 offset1:24
	ds_read2_b32 v[210:211], v124 offset0:41 offset1:57
	ds_read2_b32 v[212:213], v124 offset0:74 offset1:90
	ds_read2_b32 v[214:215], v124 offset0:107 offset1:123
	ds_read2_b32 v[216:217], v124 offset0:140 offset1:156
	ds_read2_b32 v[218:219], v124 offset0:173 offset1:189
	ds_read2_b32 v[220:221], v124 offset0:206 offset1:222
	ds_read2_b32 v[222:223], v124 offset0:239 offset1:255
	s_waitcnt lgkmcnt(12)
	v_mul_f32_e32 v192, v136, v192
	v_mul_f32_e32 v193, v136, v193
	v_mul_f32_e32 v194, v137, v194
	v_mul_f32_e32 v195, v137, v195
	v_mul_f32_e32 v196, v138, v196
	v_mul_f32_e32 v197, v138, v197
	v_mul_f32_e32 v198, v139, v198
	v_mul_f32_e32 v199, v139, v199
	v_cvt_pk_fp8_f32 v128, v192, v194
	v_cvt_pk_fp8_f32 v132, v193, v195
	s_nop 0
	v_cvt_pk_fp8_f32 v128, v196, v198 op_sel:[0,0,1]
	v_cvt_pk_fp8_f32 v132, v197, v199 op_sel:[0,0,1]
	s_waitcnt lgkmcnt(8)
	v_mul_f32_e32 v200, v140, v200
	v_mul_f32_e32 v201, v140, v201
	v_mul_f32_e32 v202, v141, v202
	v_mul_f32_e32 v203, v141, v203
	v_mul_f32_e32 v204, v142, v204
	v_mul_f32_e32 v205, v142, v205
	v_mul_f32_e32 v206, v143, v206
	v_mul_f32_e32 v207, v143, v207
	v_cvt_pk_fp8_f32 v129, v200, v202
	v_cvt_pk_fp8_f32 v133, v201, v203
	s_nop 0
	v_cvt_pk_fp8_f32 v129, v204, v206 op_sel:[0,0,1]
	v_cvt_pk_fp8_f32 v133, v205, v207 op_sel:[0,0,1]
	s_waitcnt lgkmcnt(4)
	v_mul_f32_e32 v208, v144, v208
	v_mul_f32_e32 v209, v144, v209
	v_mul_f32_e32 v210, v145, v210
	v_mul_f32_e32 v211, v145, v211
	v_mul_f32_e32 v212, v146, v212
	v_mul_f32_e32 v213, v146, v213
	v_mul_f32_e32 v214, v147, v214
	v_mul_f32_e32 v215, v147, v215
	v_cvt_pk_fp8_f32 v130, v208, v210
	v_cvt_pk_fp8_f32 v134, v209, v211
	s_nop 0
	v_cvt_pk_fp8_f32 v130, v212, v214 op_sel:[0,0,1]
	v_cvt_pk_fp8_f32 v134, v213, v215 op_sel:[0,0,1]
	s_waitcnt lgkmcnt(0)
	v_mul_f32_e32 v216, v148, v216
	v_mul_f32_e32 v217, v148, v217
	v_mul_f32_e32 v218, v149, v218
	v_mul_f32_e32 v219, v149, v219
	v_mul_f32_e32 v220, v150, v220
	v_mul_f32_e32 v221, v150, v221
	v_mul_f32_e32 v222, v151, v222
	v_mul_f32_e32 v223, v151, v223
	v_cvt_pk_fp8_f32 v131, v216, v218
	v_cvt_pk_fp8_f32 v135, v217, v219
	s_nop 0
	v_cvt_pk_fp8_f32 v131, v220, v222 op_sel:[0,0,1]
	v_cvt_pk_fp8_f32 v135, v221, v223 op_sel:[0,0,1]
	s_nop 0
	global_store_dwordx4 v120, v[128:131], s[96:97]
	global_store_dwordx4 v121, v[132:135], s[96:97]
	s_add_i32 s4, s4, s5
	s_branch .Lcv_done

.Lcv_skip:
	s_branch .LBB0_16
